# qkv occ4: B-fragment ring of three (wave id and j=1 LDS addresses recomputed instead of held in registers)
# speedup vs baseline: 1.0232x; 1.0067x over previous
_Z14k_qkv_temporalPKDF16_S0_PKfPDF16_S3_S3_PfPi:
	s_load_dwordx4 s[36:39], s[0:1], 0x0
	s_load_dwordx2 s[40:41], s[0:1], 0x10
	s_load_dwordx4 s[8:11], s[0:1], 0x30
	s_and_b32 s3, s2, 7
	s_mul_i32 s3, s3, 0x71
	s_lshr_b32 s4, s2, 3
	s_add_u32 s3, s3, s4
	s_and_b32 s22, s3, 7
	s_lshr_b32 s16, s3, 3
	s_mul_i32 s16, s16, 14
	v_lshrrev_b32_e32 v1, 6, v0
	v_and_b32_e32 v92, 15, v0
	v_bfe_u32 v90, v0, 4, 2
	v_lshlrev_b32_e32 v95, 2, v90
	v_lshl_or_b32 v91, v1, 5, v95
	v_bfe_u32 v112, v0, 3, 3
	v_and_b32_e32 v113, 7, v0
	v_lshrrev_b32_e32 v114, 1, v112
	v_and_b32_e32 v115, 1, v1
	v_lshl_or_b32 v114, v115, 2, v114
	v_xor_b32_e32 v114, v113, v114
	v_lshlrev_b32_e32 v114, 4, v114
	v_lshl_or_b32 v115, v1, 3, v112
	s_mov_b32 s42, 0x12492493
	s_movk_i32 s43, 0x627
	s_movk_i32 s44, 0x628
	v_add_u32_e32 v116, 0, v115
	v_min_u32_e32 v116, 0x7d, v116
	v_mul_hi_u32 v112, v116, s42
	v_mul_u32_u24_e32 v113, 14, v112
	v_sub_u32_e32 v113, v116, v113
	v_add_u32_e32 v113, s16, v113
	v_min_u32_e32 v113, s43, v113
	v_mad_u32_u24 v113, v112, s44, v113
	v_lshl_or_b32 v120, v113, 10, v114
	v_add_u32_e32 v116, 32, v115
	v_min_u32_e32 v116, 0x7d, v116
	v_mul_hi_u32 v112, v116, s42
	v_mul_u32_u24_e32 v113, 14, v112
	v_sub_u32_e32 v113, v116, v113
	v_add_u32_e32 v113, s16, v113
	v_min_u32_e32 v113, s43, v113
	v_mad_u32_u24 v113, v112, s44, v113
	v_lshl_or_b32 v121, v113, 10, v114
	v_add_u32_e32 v116, 64, v115
	v_min_u32_e32 v116, 0x7d, v116
	v_mul_hi_u32 v112, v116, s42
	v_mul_u32_u24_e32 v113, 14, v112
	v_sub_u32_e32 v113, v116, v113
	v_add_u32_e32 v113, s16, v113
	v_min_u32_e32 v113, s43, v113
	v_mad_u32_u24 v113, v112, s44, v113
	v_lshl_or_b32 v122, v113, 10, v114
	v_add_u32_e32 v116, 96, v115
	v_min_u32_e32 v116, 0x7d, v116
	v_mul_hi_u32 v112, v116, s42
	v_mul_u32_u24_e32 v113, 14, v112
	v_sub_u32_e32 v113, v116, v113
	v_add_u32_e32 v113, s16, v113
	v_min_u32_e32 v113, s43, v113
	v_mad_u32_u24 v113, v112, s44, v113
	v_lshl_or_b32 v123, v113, 10, v114
	v_lshlrev_b32_e32 v116, 10, v1
	s_nop 0
	v_readfirstlane_b32 s24, v116
	s_add_u32 s25, s24, 0x1000
	s_add_u32 s26, s24, 0x2000
	s_add_u32 s27, s24, 0x3000
	s_add_u32 s28, s24, 0x4000
	s_add_u32 s29, s24, 0x5000
	s_add_u32 s30, s24, 0x6000
	s_add_u32 s31, s24, 0x7000
	s_add_u32 s32, s24, 0x8000
	s_add_u32 s33, s24, 0x9000
	v_lshrrev_b32_e32 v116, 1, v92
	v_xor_b32_e32 v116, v90, v116
	v_lshlrev_b32_e32 v116, 4, v116
	v_lshl_or_b32 v94, v92, 7, v116
	v_lshlrev_b32_e32 v116, 12, v1
	v_add_u32_e32 v93, v116, v94
	s_lshl_b32 s45, s22, 6
	v_add_u32_e32 v116, s45, v115
	v_lshl_or_b32 v1, v116, 10, v114
	v_lshl_add_u32 v117, s22, 6, v92
	v_lshlrev_b32_e32 v117, 2, v117
	v_add_u32_e32 v118, 0x1000, v117
	s_waitcnt lgkmcnt(0)
	s_add_u32 s46, s38, 0x8000
	s_addc_u32 s47, s39, 0
	s_add_u32 s48, s38, 0x80000
	s_addc_u32 s49, s39, 0
	s_add_u32 s50, s38, 0x88000
	s_addc_u32 s51, s39, 0
	s_add_u32 s52, s38, 0x100000
	s_addc_u32 s53, s39, 0
	s_add_u32 s54, s38, 0x108000
	s_addc_u32 s55, s39, 0
	global_load_dword v100, v117, s[40:41] offset:0
	global_load_dword v101, v117, s[40:41] offset:64
	global_load_dword v102, v117, s[40:41] offset:128
	global_load_dword v103, v117, s[40:41] offset:192
	global_load_dword v104, v117, s[40:41] offset:2048
	global_load_dword v105, v117, s[40:41] offset:2112
	global_load_dword v106, v117, s[40:41] offset:2176
	global_load_dword v107, v117, s[40:41] offset:2240
	global_load_dword v108, v118, s[40:41] offset:0
	global_load_dword v109, v118, s[40:41] offset:64
	global_load_dword v110, v118, s[40:41] offset:128
	global_load_dword v111, v118, s[40:41] offset:192
	s_mov_b32 m0, s24
	s_nop 0
	global_load_lds_dwordx4 v120, s[36:37]
	s_mov_b32 m0, s25
	s_nop 0
	global_load_lds_dwordx4 v121, s[36:37]
	s_mov_b32 m0, s26
	s_nop 0
	global_load_lds_dwordx4 v122, s[36:37]
	s_mov_b32 m0, s27
	s_nop 0
	global_load_lds_dwordx4 v123, s[36:37]
	s_add_u32 s36, s36, 0x80
	s_addc_u32 s37, s37, 0
	s_mov_b32 m0, s28
	s_nop 0
	global_load_lds_dwordx4 v1, s[38:39]
	s_mov_b32 m0, s29
	s_nop 0
	global_load_lds_dwordx4 v1, s[46:47]
	s_mov_b32 m0, s30
	s_nop 0
	global_load_lds_dwordx4 v1, s[48:49]
	s_mov_b32 m0, s31
	s_nop 0
	global_load_lds_dwordx4 v1, s[50:51]
	s_mov_b32 m0, s32
	s_nop 0
	global_load_lds_dwordx4 v1, s[52:53]
	s_mov_b32 m0, s33
	s_nop 0
	global_load_lds_dwordx4 v1, s[54:55]
	s_add_u32 s38, s38, 0x80
	s_addc_u32 s39, s39, 0
	s_add_u32 s46, s46, 0x80
	s_addc_u32 s47, s47, 0
	s_add_u32 s48, s48, 0x80
	s_addc_u32 s49, s49, 0
	s_add_u32 s50, s50, 0x80
	s_addc_u32 s51, s51, 0
	s_add_u32 s52, s52, 0x80
	s_addc_u32 s53, s53, 0
	s_add_u32 s54, s54, 0x80
	s_addc_u32 s55, s55, 0
	s_waitcnt vmcnt(10)
	v_mov_b32_e32 v124, v100
	v_mov_b32_e32 v125, v100
	v_mov_b32_e32 v126, v100
	v_mov_b32_e32 v127, v100
	v_mov_b32_e32 v62, v100
	v_mov_b32_e32 v63, v100
	v_mov_b32_e32 v64, v100
	v_mov_b32_e32 v65, v100
	v_mov_b32_e32 v86, v101
	v_mov_b32_e32 v87, v101
	v_mov_b32_e32 v88, v101
	v_mov_b32_e32 v89, v101
	v_mov_b32_e32 v58, v101
	v_mov_b32_e32 v59, v101
	v_mov_b32_e32 v60, v101
	v_mov_b32_e32 v61, v101
	v_mov_b32_e32 v96, v102
	v_mov_b32_e32 v97, v102
	v_mov_b32_e32 v98, v102
	v_mov_b32_e32 v99, v102
	v_mov_b32_e32 v54, v102
	v_mov_b32_e32 v55, v102
	v_mov_b32_e32 v56, v102
	v_mov_b32_e32 v57, v102
	v_mov_b32_e32 v82, v103
	v_mov_b32_e32 v83, v103
	v_mov_b32_e32 v84, v103
	v_mov_b32_e32 v85, v103
	v_mov_b32_e32 v50, v103
	v_mov_b32_e32 v51, v103
	v_mov_b32_e32 v52, v103
	v_mov_b32_e32 v53, v103
	v_mov_b32_e32 v78, v104
	v_mov_b32_e32 v79, v104
	v_mov_b32_e32 v80, v104
	v_mov_b32_e32 v81, v104
	v_mov_b32_e32 v46, v104
	v_mov_b32_e32 v47, v104
	v_mov_b32_e32 v48, v104
	v_mov_b32_e32 v49, v104
	v_mov_b32_e32 v74, v105
	v_mov_b32_e32 v75, v105
	v_mov_b32_e32 v76, v105
	v_mov_b32_e32 v77, v105
	v_mov_b32_e32 v42, v105
	v_mov_b32_e32 v43, v105
	v_mov_b32_e32 v44, v105
	v_mov_b32_e32 v45, v105
	v_mov_b32_e32 v70, v106
	v_mov_b32_e32 v71, v106
	v_mov_b32_e32 v72, v106
	v_mov_b32_e32 v73, v106
	v_mov_b32_e32 v38, v106
	v_mov_b32_e32 v39, v106
	v_mov_b32_e32 v40, v106
	v_mov_b32_e32 v41, v106
	v_mov_b32_e32 v66, v107
	v_mov_b32_e32 v67, v107
	v_mov_b32_e32 v68, v107
	v_mov_b32_e32 v69, v107
	v_mov_b32_e32 v34, v107
	v_mov_b32_e32 v35, v107
	v_mov_b32_e32 v36, v107
	v_mov_b32_e32 v37, v107
	v_mov_b32_e32 v18, v108
	v_mov_b32_e32 v19, v108
	v_mov_b32_e32 v20, v108
	v_mov_b32_e32 v21, v108
	v_mov_b32_e32 v2, v108
	v_mov_b32_e32 v3, v108
	v_mov_b32_e32 v4, v108
	v_mov_b32_e32 v5, v108
	v_mov_b32_e32 v26, v109
	v_mov_b32_e32 v27, v109
	v_mov_b32_e32 v28, v109
	v_mov_b32_e32 v29, v109
	v_mov_b32_e32 v10, v109
	v_mov_b32_e32 v11, v109
	v_mov_b32_e32 v12, v109
	v_mov_b32_e32 v13, v109
	v_mov_b32_e32 v22, v110
	v_mov_b32_e32 v23, v110
	v_mov_b32_e32 v24, v110
	v_mov_b32_e32 v25, v110
	v_mov_b32_e32 v6, v110
	v_mov_b32_e32 v7, v110
	v_mov_b32_e32 v8, v110
	v_mov_b32_e32 v9, v110
	v_mov_b32_e32 v30, v111
	v_mov_b32_e32 v31, v111
	v_mov_b32_e32 v32, v111
	v_mov_b32_e32 v33, v111
	v_mov_b32_e32 v14, v111
	v_mov_b32_e32 v15, v111
	v_mov_b32_e32 v16, v111
	v_mov_b32_e32 v17, v111
	s_waitcnt vmcnt(0)
	s_barrier
	ds_read_b128 v[100:103], v93 offset:0
	ds_read_b128 v[104:107], v93 offset:2048
	ds_read_b128 v[108:111], v94 offset:16384
	ds_read_b128 v[112:115], v94 offset:18432
	ds_read_b128 v[116:119], v94 offset:20480
	s_waitcnt lgkmcnt(2)
	v_mfma_f32_16x16x32_f16 v[124:127], v[100:103], v[108:111], v[124:127]
	v_mfma_f32_16x16x32_f16 v[62:65], v[104:107], v[108:111], v[62:65]
	ds_read_b128 v[108:111], v94 offset:22528
	s_waitcnt lgkmcnt(2)
	v_mfma_f32_16x16x32_f16 v[86:89], v[100:103], v[112:115], v[86:89]
	v_mfma_f32_16x16x32_f16 v[58:61], v[104:107], v[112:115], v[58:61]
	ds_read_b128 v[112:115], v94 offset:24576
	s_waitcnt lgkmcnt(2)
	v_mfma_f32_16x16x32_f16 v[96:99], v[100:103], v[116:119], v[96:99]
	v_mfma_f32_16x16x32_f16 v[54:57], v[104:107], v[116:119], v[54:57]
	ds_read_b128 v[116:119], v94 offset:26624
	s_waitcnt lgkmcnt(2)
	v_mfma_f32_16x16x32_f16 v[82:85], v[100:103], v[108:111], v[82:85]
	v_mfma_f32_16x16x32_f16 v[50:53], v[104:107], v[108:111], v[50:53]
	ds_read_b128 v[108:111], v94 offset:28672
	s_waitcnt lgkmcnt(2)
	v_mfma_f32_16x16x32_f16 v[78:81], v[100:103], v[112:115], v[78:81]
	v_mfma_f32_16x16x32_f16 v[46:49], v[104:107], v[112:115], v[46:49]
	ds_read_b128 v[112:115], v94 offset:30720
	s_waitcnt lgkmcnt(2)
	v_mfma_f32_16x16x32_f16 v[74:77], v[100:103], v[116:119], v[74:77]
	v_mfma_f32_16x16x32_f16 v[42:45], v[104:107], v[116:119], v[42:45]
	ds_read_b128 v[116:119], v94 offset:32768
	s_waitcnt lgkmcnt(2)
	v_mfma_f32_16x16x32_f16 v[70:73], v[100:103], v[108:111], v[70:73]
	v_mfma_f32_16x16x32_f16 v[38:41], v[104:107], v[108:111], v[38:41]
	ds_read_b128 v[108:111], v94 offset:34816
	s_waitcnt lgkmcnt(2)
	v_mfma_f32_16x16x32_f16 v[66:69], v[100:103], v[112:115], v[66:69]
	v_mfma_f32_16x16x32_f16 v[34:37], v[104:107], v[112:115], v[34:37]
	ds_read_b128 v[112:115], v94 offset:36864
	s_waitcnt lgkmcnt(2)
	v_mfma_f32_16x16x32_f16 v[18:21], v[100:103], v[116:119], v[18:21]
	v_mfma_f32_16x16x32_f16 v[2:5], v[104:107], v[116:119], v[2:5]
	ds_read_b128 v[116:119], v94 offset:38912
	s_waitcnt lgkmcnt(2)
	v_mfma_f32_16x16x32_f16 v[26:29], v[100:103], v[108:111], v[26:29]
	v_mfma_f32_16x16x32_f16 v[10:13], v[104:107], v[108:111], v[10:13]
	v_xor_b32_e32 v94, 64, v94
	ds_read_b128 v[108:111], v94 offset:16384
	s_waitcnt lgkmcnt(2)
	v_mfma_f32_16x16x32_f16 v[22:25], v[100:103], v[112:115], v[22:25]
	v_mfma_f32_16x16x32_f16 v[6:9], v[104:107], v[112:115], v[6:9]
	ds_read_b128 v[112:115], v94 offset:18432
	s_waitcnt lgkmcnt(2)
	v_mfma_f32_16x16x32_f16 v[30:33], v[100:103], v[116:119], v[30:33]
	v_mfma_f32_16x16x32_f16 v[14:17], v[104:107], v[116:119], v[14:17]
	ds_read_b128 v[116:119], v94 offset:20480
	v_xor_b32_e32 v93, 64, v93
	ds_read_b128 v[100:103], v93 offset:0
	ds_read_b128 v[104:107], v93 offset:2048
	v_xor_b32_e32 v93, 64, v93
	s_waitcnt lgkmcnt(0)
	v_mfma_f32_16x16x32_f16 v[124:127], v[100:103], v[108:111], v[124:127]
	v_mfma_f32_16x16x32_f16 v[62:65], v[104:107], v[108:111], v[62:65]
	ds_read_b128 v[108:111], v94 offset:22528
	s_waitcnt lgkmcnt(1)
	v_mfma_f32_16x16x32_f16 v[86:89], v[100:103], v[112:115], v[86:89]
	v_mfma_f32_16x16x32_f16 v[58:61], v[104:107], v[112:115], v[58:61]
	ds_read_b128 v[112:115], v94 offset:24576
	s_waitcnt lgkmcnt(2)
	v_mfma_f32_16x16x32_f16 v[96:99], v[100:103], v[116:119], v[96:99]
	v_mfma_f32_16x16x32_f16 v[54:57], v[104:107], v[116:119], v[54:57]
	ds_read_b128 v[116:119], v94 offset:26624
	s_waitcnt lgkmcnt(2)
	v_mfma_f32_16x16x32_f16 v[82:85], v[100:103], v[108:111], v[82:85]
	v_mfma_f32_16x16x32_f16 v[50:53], v[104:107], v[108:111], v[50:53]
	ds_read_b128 v[108:111], v94 offset:28672
	s_waitcnt lgkmcnt(2)
	v_mfma_f32_16x16x32_f16 v[78:81], v[100:103], v[112:115], v[78:81]
	v_mfma_f32_16x16x32_f16 v[46:49], v[104:107], v[112:115], v[46:49]
	ds_read_b128 v[112:115], v94 offset:30720
	s_waitcnt lgkmcnt(2)
	v_mfma_f32_16x16x32_f16 v[74:77], v[100:103], v[116:119], v[74:77]
	v_mfma_f32_16x16x32_f16 v[42:45], v[104:107], v[116:119], v[42:45]
	ds_read_b128 v[116:119], v94 offset:32768
	s_waitcnt lgkmcnt(2)
	v_mfma_f32_16x16x32_f16 v[70:73], v[100:103], v[108:111], v[70:73]
	v_mfma_f32_16x16x32_f16 v[38:41], v[104:107], v[108:111], v[38:41]
	ds_read_b128 v[108:111], v94 offset:34816
	s_waitcnt lgkmcnt(2)
	v_mfma_f32_16x16x32_f16 v[66:69], v[100:103], v[112:115], v[66:69]
	v_mfma_f32_16x16x32_f16 v[34:37], v[104:107], v[112:115], v[34:37]
	ds_read_b128 v[112:115], v94 offset:36864
	s_waitcnt lgkmcnt(2)
	v_mfma_f32_16x16x32_f16 v[18:21], v[100:103], v[116:119], v[18:21]
	v_mfma_f32_16x16x32_f16 v[2:5], v[104:107], v[116:119], v[2:5]
	ds_read_b128 v[116:119], v94 offset:38912
	v_xor_b32_e32 v94, 64, v94
	s_waitcnt lgkmcnt(0)
	s_barrier
	s_mov_b32 m0, s24
	s_nop 0
	global_load_lds_dwordx4 v120, s[36:37]
	s_mov_b32 m0, s25
	s_nop 0
	global_load_lds_dwordx4 v121, s[36:37]
	s_mov_b32 m0, s26
	s_nop 0
	global_load_lds_dwordx4 v122, s[36:37]
	s_mov_b32 m0, s27
	s_nop 0
	global_load_lds_dwordx4 v123, s[36:37]
	s_add_u32 s36, s36, 0x80
	s_addc_u32 s37, s37, 0
	s_mov_b32 m0, s28
	s_nop 0
	global_load_lds_dwordx4 v1, s[38:39]
	s_mov_b32 m0, s29
	s_nop 0
	global_load_lds_dwordx4 v1, s[46:47]
	s_mov_b32 m0, s30
	s_nop 0
	global_load_lds_dwordx4 v1, s[48:49]
	s_mov_b32 m0, s31
	s_nop 0
	global_load_lds_dwordx4 v1, s[50:51]
	s_mov_b32 m0, s32
	s_nop 0
	global_load_lds_dwordx4 v1, s[52:53]
	s_mov_b32 m0, s33
	s_nop 0
	global_load_lds_dwordx4 v1, s[54:55]
	s_add_u32 s38, s38, 0x80
	s_addc_u32 s39, s39, 0
	s_add_u32 s46, s46, 0x80
	s_addc_u32 s47, s47, 0
	s_add_u32 s48, s48, 0x80
	s_addc_u32 s49, s49, 0
	s_add_u32 s50, s50, 0x80
	s_addc_u32 s51, s51, 0
	s_add_u32 s52, s52, 0x80
	s_addc_u32 s53, s53, 0
	s_add_u32 s54, s54, 0x80
	s_addc_u32 s55, s55, 0
	s_waitcnt lgkmcnt(2)
	v_mfma_f32_16x16x32_f16 v[26:29], v[100:103], v[108:111], v[26:29]
	v_mfma_f32_16x16x32_f16 v[10:13], v[104:107], v[108:111], v[10:13]
	s_waitcnt lgkmcnt(1)
	v_mfma_f32_16x16x32_f16 v[22:25], v[100:103], v[112:115], v[22:25]
	v_mfma_f32_16x16x32_f16 v[6:9], v[104:107], v[112:115], v[6:9]
	s_waitcnt lgkmcnt(0)
	v_mfma_f32_16x16x32_f16 v[30:33], v[100:103], v[116:119], v[30:33]
	v_mfma_f32_16x16x32_f16 v[14:17], v[104:107], v[116:119], v[14:17]
	s_waitcnt vmcnt(0)
	s_barrier
	ds_read_b128 v[100:103], v93 offset:0
	ds_read_b128 v[104:107], v93 offset:2048
	ds_read_b128 v[108:111], v94 offset:16384
	ds_read_b128 v[112:115], v94 offset:18432
	ds_read_b128 v[116:119], v94 offset:20480
	s_waitcnt lgkmcnt(2)
	v_mfma_f32_16x16x32_f16 v[124:127], v[100:103], v[108:111], v[124:127]
	v_mfma_f32_16x16x32_f16 v[62:65], v[104:107], v[108:111], v[62:65]
	ds_read_b128 v[108:111], v94 offset:22528
	s_waitcnt lgkmcnt(2)
	v_mfma_f32_16x16x32_f16 v[86:89], v[100:103], v[112:115], v[86:89]
	v_mfma_f32_16x16x32_f16 v[58:61], v[104:107], v[112:115], v[58:61]
	ds_read_b128 v[112:115], v94 offset:24576
	s_waitcnt lgkmcnt(2)
	v_mfma_f32_16x16x32_f16 v[96:99], v[100:103], v[116:119], v[96:99]
	v_mfma_f32_16x16x32_f16 v[54:57], v[104:107], v[116:119], v[54:57]
	ds_read_b128 v[116:119], v94 offset:26624
	s_waitcnt lgkmcnt(2)
	v_mfma_f32_16x16x32_f16 v[82:85], v[100:103], v[108:111], v[82:85]
	v_mfma_f32_16x16x32_f16 v[50:53], v[104:107], v[108:111], v[50:53]
	ds_read_b128 v[108:111], v94 offset:28672
	s_waitcnt lgkmcnt(2)
	v_mfma_f32_16x16x32_f16 v[78:81], v[100:103], v[112:115], v[78:81]
	v_mfma_f32_16x16x32_f16 v[46:49], v[104:107], v[112:115], v[46:49]
	ds_read_b128 v[112:115], v94 offset:30720
	s_waitcnt lgkmcnt(2)
	v_mfma_f32_16x16x32_f16 v[74:77], v[100:103], v[116:119], v[74:77]
	v_mfma_f32_16x16x32_f16 v[42:45], v[104:107], v[116:119], v[42:45]
	ds_read_b128 v[116:119], v94 offset:32768
	s_waitcnt lgkmcnt(2)
	v_mfma_f32_16x16x32_f16 v[70:73], v[100:103], v[108:111], v[70:73]
	v_mfma_f32_16x16x32_f16 v[38:41], v[104:107], v[108:111], v[38:41]
	ds_read_b128 v[108:111], v94 offset:34816
	s_waitcnt lgkmcnt(2)
	v_mfma_f32_16x16x32_f16 v[66:69], v[100:103], v[112:115], v[66:69]
	v_mfma_f32_16x16x32_f16 v[34:37], v[104:107], v[112:115], v[34:37]
	ds_read_b128 v[112:115], v94 offset:36864
	s_waitcnt lgkmcnt(2)
	v_mfma_f32_16x16x32_f16 v[18:21], v[100:103], v[116:119], v[18:21]
	v_mfma_f32_16x16x32_f16 v[2:5], v[104:107], v[116:119], v[2:5]
	ds_read_b128 v[116:119], v94 offset:38912
	s_waitcnt lgkmcnt(2)
	v_mfma_f32_16x16x32_f16 v[26:29], v[100:103], v[108:111], v[26:29]
	v_mfma_f32_16x16x32_f16 v[10:13], v[104:107], v[108:111], v[10:13]
	v_xor_b32_e32 v94, 64, v94
	ds_read_b128 v[108:111], v94 offset:16384
	s_waitcnt lgkmcnt(2)
	v_mfma_f32_16x16x32_f16 v[22:25], v[100:103], v[112:115], v[22:25]
	v_mfma_f32_16x16x32_f16 v[6:9], v[104:107], v[112:115], v[6:9]
	ds_read_b128 v[112:115], v94 offset:18432
	s_waitcnt lgkmcnt(2)
	v_mfma_f32_16x16x32_f16 v[30:33], v[100:103], v[116:119], v[30:33]
	v_mfma_f32_16x16x32_f16 v[14:17], v[104:107], v[116:119], v[14:17]
	ds_read_b128 v[116:119], v94 offset:20480
	v_xor_b32_e32 v93, 64, v93
	ds_read_b128 v[100:103], v93 offset:0
	ds_read_b128 v[104:107], v93 offset:2048
	v_xor_b32_e32 v93, 64, v93
	s_waitcnt lgkmcnt(0)
	v_mfma_f32_16x16x32_f16 v[124:127], v[100:103], v[108:111], v[124:127]
	v_mfma_f32_16x16x32_f16 v[62:65], v[104:107], v[108:111], v[62:65]
	ds_read_b128 v[108:111], v94 offset:22528
	s_waitcnt lgkmcnt(1)
	v_mfma_f32_16x16x32_f16 v[86:89], v[100:103], v[112:115], v[86:89]
	v_mfma_f32_16x16x32_f16 v[58:61], v[104:107], v[112:115], v[58:61]
	ds_read_b128 v[112:115], v94 offset:24576
	s_waitcnt lgkmcnt(2)
	v_mfma_f32_16x16x32_f16 v[96:99], v[100:103], v[116:119], v[96:99]
	v_mfma_f32_16x16x32_f16 v[54:57], v[104:107], v[116:119], v[54:57]
	ds_read_b128 v[116:119], v94 offset:26624
	s_waitcnt lgkmcnt(2)
	v_mfma_f32_16x16x32_f16 v[82:85], v[100:103], v[108:111], v[82:85]
	v_mfma_f32_16x16x32_f16 v[50:53], v[104:107], v[108:111], v[50:53]
	ds_read_b128 v[108:111], v94 offset:28672
	s_waitcnt lgkmcnt(2)
	v_mfma_f32_16x16x32_f16 v[78:81], v[100:103], v[112:115], v[78:81]
	v_mfma_f32_16x16x32_f16 v[46:49], v[104:107], v[112:115], v[46:49]
	ds_read_b128 v[112:115], v94 offset:30720
	s_waitcnt lgkmcnt(2)
	v_mfma_f32_16x16x32_f16 v[74:77], v[100:103], v[116:119], v[74:77]
	v_mfma_f32_16x16x32_f16 v[42:45], v[104:107], v[116:119], v[42:45]
	ds_read_b128 v[116:119], v94 offset:32768
	s_waitcnt lgkmcnt(2)
	v_mfma_f32_16x16x32_f16 v[70:73], v[100:103], v[108:111], v[70:73]
	v_mfma_f32_16x16x32_f16 v[38:41], v[104:107], v[108:111], v[38:41]
	ds_read_b128 v[108:111], v94 offset:34816
	s_waitcnt lgkmcnt(2)
	v_mfma_f32_16x16x32_f16 v[66:69], v[100:103], v[112:115], v[66:69]
	v_mfma_f32_16x16x32_f16 v[34:37], v[104:107], v[112:115], v[34:37]
	ds_read_b128 v[112:115], v94 offset:36864
	s_waitcnt lgkmcnt(2)
	v_mfma_f32_16x16x32_f16 v[18:21], v[100:103], v[116:119], v[18:21]
	v_mfma_f32_16x16x32_f16 v[2:5], v[104:107], v[116:119], v[2:5]
	ds_read_b128 v[116:119], v94 offset:38912
	v_xor_b32_e32 v94, 64, v94
	s_waitcnt lgkmcnt(0)
	s_barrier
	s_mov_b32 m0, s24
	s_nop 0
	global_load_lds_dwordx4 v120, s[36:37]
	s_mov_b32 m0, s25
	s_nop 0
	global_load_lds_dwordx4 v121, s[36:37]
	s_mov_b32 m0, s26
	s_nop 0
	global_load_lds_dwordx4 v122, s[36:37]
	s_mov_b32 m0, s27
	s_nop 0
	global_load_lds_dwordx4 v123, s[36:37]
	s_add_u32 s36, s36, 0x80
	s_addc_u32 s37, s37, 0
	s_mov_b32 m0, s28
	s_nop 0
	global_load_lds_dwordx4 v1, s[38:39]
	s_mov_b32 m0, s29
	s_nop 0
	global_load_lds_dwordx4 v1, s[46:47]
	s_mov_b32 m0, s30
	s_nop 0
	global_load_lds_dwordx4 v1, s[48:49]
	s_mov_b32 m0, s31
	s_nop 0
	global_load_lds_dwordx4 v1, s[50:51]
	s_mov_b32 m0, s32
	s_nop 0
	global_load_lds_dwordx4 v1, s[52:53]
	s_mov_b32 m0, s33
	s_nop 0
	global_load_lds_dwordx4 v1, s[54:55]
	s_add_u32 s38, s38, 0x80
	s_addc_u32 s39, s39, 0
	s_add_u32 s46, s46, 0x80
	s_addc_u32 s47, s47, 0
	s_add_u32 s48, s48, 0x80
	s_addc_u32 s49, s49, 0
	s_add_u32 s50, s50, 0x80
	s_addc_u32 s51, s51, 0
	s_add_u32 s52, s52, 0x80
	s_addc_u32 s53, s53, 0
	s_add_u32 s54, s54, 0x80
	s_addc_u32 s55, s55, 0
	s_waitcnt lgkmcnt(2)
	v_mfma_f32_16x16x32_f16 v[26:29], v[100:103], v[108:111], v[26:29]
	v_mfma_f32_16x16x32_f16 v[10:13], v[104:107], v[108:111], v[10:13]
	s_waitcnt lgkmcnt(1)
	v_mfma_f32_16x16x32_f16 v[22:25], v[100:103], v[112:115], v[22:25]
	v_mfma_f32_16x16x32_f16 v[6:9], v[104:107], v[112:115], v[6:9]
	s_waitcnt lgkmcnt(0)
	v_mfma_f32_16x16x32_f16 v[30:33], v[100:103], v[116:119], v[30:33]
	v_mfma_f32_16x16x32_f16 v[14:17], v[104:107], v[116:119], v[14:17]
	s_waitcnt vmcnt(0)
	s_barrier
	ds_read_b128 v[100:103], v93 offset:0
	ds_read_b128 v[104:107], v93 offset:2048
	ds_read_b128 v[108:111], v94 offset:16384
	ds_read_b128 v[112:115], v94 offset:18432
	ds_read_b128 v[116:119], v94 offset:20480
	s_waitcnt lgkmcnt(2)
	v_mfma_f32_16x16x32_f16 v[124:127], v[100:103], v[108:111], v[124:127]
	v_mfma_f32_16x16x32_f16 v[62:65], v[104:107], v[108:111], v[62:65]
	ds_read_b128 v[108:111], v94 offset:22528
	s_waitcnt lgkmcnt(2)
	v_mfma_f32_16x16x32_f16 v[86:89], v[100:103], v[112:115], v[86:89]
	v_mfma_f32_16x16x32_f16 v[58:61], v[104:107], v[112:115], v[58:61]
	ds_read_b128 v[112:115], v94 offset:24576
	s_waitcnt lgkmcnt(2)
	v_mfma_f32_16x16x32_f16 v[96:99], v[100:103], v[116:119], v[96:99]
	v_mfma_f32_16x16x32_f16 v[54:57], v[104:107], v[116:119], v[54:57]
	ds_read_b128 v[116:119], v94 offset:26624
	s_waitcnt lgkmcnt(2)
	v_mfma_f32_16x16x32_f16 v[82:85], v[100:103], v[108:111], v[82:85]
	v_mfma_f32_16x16x32_f16 v[50:53], v[104:107], v[108:111], v[50:53]
	ds_read_b128 v[108:111], v94 offset:28672
	s_waitcnt lgkmcnt(2)
	v_mfma_f32_16x16x32_f16 v[78:81], v[100:103], v[112:115], v[78:81]
	v_mfma_f32_16x16x32_f16 v[46:49], v[104:107], v[112:115], v[46:49]
	ds_read_b128 v[112:115], v94 offset:30720
	s_waitcnt lgkmcnt(2)
	v_mfma_f32_16x16x32_f16 v[74:77], v[100:103], v[116:119], v[74:77]
	v_mfma_f32_16x16x32_f16 v[42:45], v[104:107], v[116:119], v[42:45]
	ds_read_b128 v[116:119], v94 offset:32768
	s_waitcnt lgkmcnt(2)
	v_mfma_f32_16x16x32_f16 v[70:73], v[100:103], v[108:111], v[70:73]
	v_mfma_f32_16x16x32_f16 v[38:41], v[104:107], v[108:111], v[38:41]
	ds_read_b128 v[108:111], v94 offset:34816
	s_waitcnt lgkmcnt(2)
	v_mfma_f32_16x16x32_f16 v[66:69], v[100:103], v[112:115], v[66:69]
	v_mfma_f32_16x16x32_f16 v[34:37], v[104:107], v[112:115], v[34:37]
	ds_read_b128 v[112:115], v94 offset:36864
	s_waitcnt lgkmcnt(2)
	v_mfma_f32_16x16x32_f16 v[18:21], v[100:103], v[116:119], v[18:21]
	v_mfma_f32_16x16x32_f16 v[2:5], v[104:107], v[116:119], v[2:5]
	ds_read_b128 v[116:119], v94 offset:38912
	s_waitcnt lgkmcnt(2)
	v_mfma_f32_16x16x32_f16 v[26:29], v[100:103], v[108:111], v[26:29]
	v_mfma_f32_16x16x32_f16 v[10:13], v[104:107], v[108:111], v[10:13]
	v_xor_b32_e32 v94, 64, v94
	ds_read_b128 v[108:111], v94 offset:16384
	s_waitcnt lgkmcnt(2)
	v_mfma_f32_16x16x32_f16 v[22:25], v[100:103], v[112:115], v[22:25]
	v_mfma_f32_16x16x32_f16 v[6:9], v[104:107], v[112:115], v[6:9]
	ds_read_b128 v[112:115], v94 offset:18432
	s_waitcnt lgkmcnt(2)
	v_mfma_f32_16x16x32_f16 v[30:33], v[100:103], v[116:119], v[30:33]
	v_mfma_f32_16x16x32_f16 v[14:17], v[104:107], v[116:119], v[14:17]
	ds_read_b128 v[116:119], v94 offset:20480
	v_xor_b32_e32 v93, 64, v93
	ds_read_b128 v[100:103], v93 offset:0
	ds_read_b128 v[104:107], v93 offset:2048
	v_xor_b32_e32 v93, 64, v93
	s_waitcnt lgkmcnt(0)
	v_mfma_f32_16x16x32_f16 v[124:127], v[100:103], v[108:111], v[124:127]
	v_mfma_f32_16x16x32_f16 v[62:65], v[104:107], v[108:111], v[62:65]
	ds_read_b128 v[108:111], v94 offset:22528
	s_waitcnt lgkmcnt(1)
	v_mfma_f32_16x16x32_f16 v[86:89], v[100:103], v[112:115], v[86:89]
	v_mfma_f32_16x16x32_f16 v[58:61], v[104:107], v[112:115], v[58:61]
	ds_read_b128 v[112:115], v94 offset:24576
	s_waitcnt lgkmcnt(2)
	v_mfma_f32_16x16x32_f16 v[96:99], v[100:103], v[116:119], v[96:99]
	v_mfma_f32_16x16x32_f16 v[54:57], v[104:107], v[116:119], v[54:57]
	ds_read_b128 v[116:119], v94 offset:26624
	s_waitcnt lgkmcnt(2)
	v_mfma_f32_16x16x32_f16 v[82:85], v[100:103], v[108:111], v[82:85]
	v_mfma_f32_16x16x32_f16 v[50:53], v[104:107], v[108:111], v[50:53]
	ds_read_b128 v[108:111], v94 offset:28672
	s_waitcnt lgkmcnt(2)
	v_mfma_f32_16x16x32_f16 v[78:81], v[100:103], v[112:115], v[78:81]
	v_mfma_f32_16x16x32_f16 v[46:49], v[104:107], v[112:115], v[46:49]
	ds_read_b128 v[112:115], v94 offset:30720
	s_waitcnt lgkmcnt(2)
	v_mfma_f32_16x16x32_f16 v[74:77], v[100:103], v[116:119], v[74:77]
	v_mfma_f32_16x16x32_f16 v[42:45], v[104:107], v[116:119], v[42:45]
	ds_read_b128 v[116:119], v94 offset:32768
	s_waitcnt lgkmcnt(2)
	v_mfma_f32_16x16x32_f16 v[70:73], v[100:103], v[108:111], v[70:73]
	v_mfma_f32_16x16x32_f16 v[38:41], v[104:107], v[108:111], v[38:41]
	ds_read_b128 v[108:111], v94 offset:34816
	s_waitcnt lgkmcnt(2)
	v_mfma_f32_16x16x32_f16 v[66:69], v[100:103], v[112:115], v[66:69]
	v_mfma_f32_16x16x32_f16 v[34:37], v[104:107], v[112:115], v[34:37]
	ds_read_b128 v[112:115], v94 offset:36864
	s_waitcnt lgkmcnt(2)
	v_mfma_f32_16x16x32_f16 v[18:21], v[100:103], v[116:119], v[18:21]
	v_mfma_f32_16x16x32_f16 v[2:5], v[104:107], v[116:119], v[2:5]
	ds_read_b128 v[116:119], v94 offset:38912
	v_xor_b32_e32 v94, 64, v94
	s_waitcnt lgkmcnt(0)
	s_barrier
	s_mov_b32 m0, s24
	s_nop 0
	global_load_lds_dwordx4 v120, s[36:37]
	s_mov_b32 m0, s25
	s_nop 0
	global_load_lds_dwordx4 v121, s[36:37]
	s_mov_b32 m0, s26
	s_nop 0
	global_load_lds_dwordx4 v122, s[36:37]
	s_mov_b32 m0, s27
	s_nop 0
	global_load_lds_dwordx4 v123, s[36:37]
	s_add_u32 s36, s36, 0x80
	s_addc_u32 s37, s37, 0
	s_mov_b32 m0, s28
	s_nop 0
	global_load_lds_dwordx4 v1, s[38:39]
	s_mov_b32 m0, s29
	s_nop 0
	global_load_lds_dwordx4 v1, s[46:47]
	s_mov_b32 m0, s30
	s_nop 0
	global_load_lds_dwordx4 v1, s[48:49]
	s_mov_b32 m0, s31
	s_nop 0
	global_load_lds_dwordx4 v1, s[50:51]
	s_mov_b32 m0, s32
	s_nop 0
	global_load_lds_dwordx4 v1, s[52:53]
	s_mov_b32 m0, s33
	s_nop 0
	global_load_lds_dwordx4 v1, s[54:55]
	s_add_u32 s38, s38, 0x80
	s_addc_u32 s39, s39, 0
	s_add_u32 s46, s46, 0x80
	s_addc_u32 s47, s47, 0
	s_add_u32 s48, s48, 0x80
	s_addc_u32 s49, s49, 0
	s_add_u32 s50, s50, 0x80
	s_addc_u32 s51, s51, 0
	s_add_u32 s52, s52, 0x80
	s_addc_u32 s53, s53, 0
	s_add_u32 s54, s54, 0x80
	s_addc_u32 s55, s55, 0
	s_waitcnt lgkmcnt(2)
	v_mfma_f32_16x16x32_f16 v[26:29], v[100:103], v[108:111], v[26:29]
	v_mfma_f32_16x16x32_f16 v[10:13], v[104:107], v[108:111], v[10:13]
	s_waitcnt lgkmcnt(1)
	v_mfma_f32_16x16x32_f16 v[22:25], v[100:103], v[112:115], v[22:25]
	v_mfma_f32_16x16x32_f16 v[6:9], v[104:107], v[112:115], v[6:9]
	s_waitcnt lgkmcnt(0)
	v_mfma_f32_16x16x32_f16 v[30:33], v[100:103], v[116:119], v[30:33]
	v_mfma_f32_16x16x32_f16 v[14:17], v[104:107], v[116:119], v[14:17]
	s_waitcnt vmcnt(0)
	s_barrier
	ds_read_b128 v[100:103], v93 offset:0
	ds_read_b128 v[104:107], v93 offset:2048
	ds_read_b128 v[108:111], v94 offset:16384
	ds_read_b128 v[112:115], v94 offset:18432
	ds_read_b128 v[116:119], v94 offset:20480
	s_waitcnt lgkmcnt(2)
	v_mfma_f32_16x16x32_f16 v[124:127], v[100:103], v[108:111], v[124:127]
	v_mfma_f32_16x16x32_f16 v[62:65], v[104:107], v[108:111], v[62:65]
	ds_read_b128 v[108:111], v94 offset:22528
	s_waitcnt lgkmcnt(2)
	v_mfma_f32_16x16x32_f16 v[86:89], v[100:103], v[112:115], v[86:89]
	v_mfma_f32_16x16x32_f16 v[58:61], v[104:107], v[112:115], v[58:61]
	ds_read_b128 v[112:115], v94 offset:24576
	s_waitcnt lgkmcnt(2)
	v_mfma_f32_16x16x32_f16 v[96:99], v[100:103], v[116:119], v[96:99]
	v_mfma_f32_16x16x32_f16 v[54:57], v[104:107], v[116:119], v[54:57]
	ds_read_b128 v[116:119], v94 offset:26624
	s_waitcnt lgkmcnt(2)
	v_mfma_f32_16x16x32_f16 v[82:85], v[100:103], v[108:111], v[82:85]
	v_mfma_f32_16x16x32_f16 v[50:53], v[104:107], v[108:111], v[50:53]
	ds_read_b128 v[108:111], v94 offset:28672
	s_waitcnt lgkmcnt(2)
	v_mfma_f32_16x16x32_f16 v[78:81], v[100:103], v[112:115], v[78:81]
	v_mfma_f32_16x16x32_f16 v[46:49], v[104:107], v[112:115], v[46:49]
	ds_read_b128 v[112:115], v94 offset:30720
	s_waitcnt lgkmcnt(2)
	v_mfma_f32_16x16x32_f16 v[74:77], v[100:103], v[116:119], v[74:77]
	v_mfma_f32_16x16x32_f16 v[42:45], v[104:107], v[116:119], v[42:45]
	ds_read_b128 v[116:119], v94 offset:32768
	s_waitcnt lgkmcnt(2)
	v_mfma_f32_16x16x32_f16 v[70:73], v[100:103], v[108:111], v[70:73]
	v_mfma_f32_16x16x32_f16 v[38:41], v[104:107], v[108:111], v[38:41]
	ds_read_b128 v[108:111], v94 offset:34816
	s_waitcnt lgkmcnt(2)
	v_mfma_f32_16x16x32_f16 v[66:69], v[100:103], v[112:115], v[66:69]
	v_mfma_f32_16x16x32_f16 v[34:37], v[104:107], v[112:115], v[34:37]
	ds_read_b128 v[112:115], v94 offset:36864
	s_waitcnt lgkmcnt(2)
	v_mfma_f32_16x16x32_f16 v[18:21], v[100:103], v[116:119], v[18:21]
	v_mfma_f32_16x16x32_f16 v[2:5], v[104:107], v[116:119], v[2:5]
	ds_read_b128 v[116:119], v94 offset:38912
	s_waitcnt lgkmcnt(2)
	v_mfma_f32_16x16x32_f16 v[26:29], v[100:103], v[108:111], v[26:29]
	v_mfma_f32_16x16x32_f16 v[10:13], v[104:107], v[108:111], v[10:13]
	v_xor_b32_e32 v94, 64, v94
	ds_read_b128 v[108:111], v94 offset:16384
	s_waitcnt lgkmcnt(2)
	v_mfma_f32_16x16x32_f16 v[22:25], v[100:103], v[112:115], v[22:25]
	v_mfma_f32_16x16x32_f16 v[6:9], v[104:107], v[112:115], v[6:9]
	ds_read_b128 v[112:115], v94 offset:18432
	s_waitcnt lgkmcnt(2)
	v_mfma_f32_16x16x32_f16 v[30:33], v[100:103], v[116:119], v[30:33]
	v_mfma_f32_16x16x32_f16 v[14:17], v[104:107], v[116:119], v[14:17]
	ds_read_b128 v[116:119], v94 offset:20480
	v_xor_b32_e32 v93, 64, v93
	ds_read_b128 v[100:103], v93 offset:0
	ds_read_b128 v[104:107], v93 offset:2048
	v_xor_b32_e32 v93, 64, v93
	s_waitcnt lgkmcnt(0)
	v_mfma_f32_16x16x32_f16 v[124:127], v[100:103], v[108:111], v[124:127]
	v_mfma_f32_16x16x32_f16 v[62:65], v[104:107], v[108:111], v[62:65]
	ds_read_b128 v[108:111], v94 offset:22528
	s_waitcnt lgkmcnt(1)
	v_mfma_f32_16x16x32_f16 v[86:89], v[100:103], v[112:115], v[86:89]
	v_mfma_f32_16x16x32_f16 v[58:61], v[104:107], v[112:115], v[58:61]
	ds_read_b128 v[112:115], v94 offset:24576
	s_waitcnt lgkmcnt(2)
	v_mfma_f32_16x16x32_f16 v[96:99], v[100:103], v[116:119], v[96:99]
	v_mfma_f32_16x16x32_f16 v[54:57], v[104:107], v[116:119], v[54:57]
	ds_read_b128 v[116:119], v94 offset:26624
	s_waitcnt lgkmcnt(2)
	v_mfma_f32_16x16x32_f16 v[82:85], v[100:103], v[108:111], v[82:85]
	v_mfma_f32_16x16x32_f16 v[50:53], v[104:107], v[108:111], v[50:53]
	ds_read_b128 v[108:111], v94 offset:28672
	s_waitcnt lgkmcnt(2)
	v_mfma_f32_16x16x32_f16 v[78:81], v[100:103], v[112:115], v[78:81]
	v_mfma_f32_16x16x32_f16 v[46:49], v[104:107], v[112:115], v[46:49]
	ds_read_b128 v[112:115], v94 offset:30720
	s_waitcnt lgkmcnt(2)
	v_mfma_f32_16x16x32_f16 v[74:77], v[100:103], v[116:119], v[74:77]
	v_mfma_f32_16x16x32_f16 v[42:45], v[104:107], v[116:119], v[42:45]
	ds_read_b128 v[116:119], v94 offset:32768
	s_waitcnt lgkmcnt(2)
	v_mfma_f32_16x16x32_f16 v[70:73], v[100:103], v[108:111], v[70:73]
	v_mfma_f32_16x16x32_f16 v[38:41], v[104:107], v[108:111], v[38:41]
	ds_read_b128 v[108:111], v94 offset:34816
	s_waitcnt lgkmcnt(2)
	v_mfma_f32_16x16x32_f16 v[66:69], v[100:103], v[112:115], v[66:69]
	v_mfma_f32_16x16x32_f16 v[34:37], v[104:107], v[112:115], v[34:37]
	ds_read_b128 v[112:115], v94 offset:36864
	s_waitcnt lgkmcnt(2)
	v_mfma_f32_16x16x32_f16 v[18:21], v[100:103], v[116:119], v[18:21]
	v_mfma_f32_16x16x32_f16 v[2:5], v[104:107], v[116:119], v[2:5]
	ds_read_b128 v[116:119], v94 offset:38912
	v_xor_b32_e32 v94, 64, v94
	s_waitcnt lgkmcnt(0)
	s_barrier
	s_mov_b32 m0, s24
	s_nop 0
	global_load_lds_dwordx4 v120, s[36:37]
	s_mov_b32 m0, s25
	s_nop 0
	global_load_lds_dwordx4 v121, s[36:37]
	s_mov_b32 m0, s26
	s_nop 0
	global_load_lds_dwordx4 v122, s[36:37]
	s_mov_b32 m0, s27
	s_nop 0
	global_load_lds_dwordx4 v123, s[36:37]
	s_add_u32 s36, s36, 0x80
	s_addc_u32 s37, s37, 0
	s_mov_b32 m0, s28
	s_nop 0
	global_load_lds_dwordx4 v1, s[38:39]
	s_mov_b32 m0, s29
	s_nop 0
	global_load_lds_dwordx4 v1, s[46:47]
	s_mov_b32 m0, s30
	s_nop 0
	global_load_lds_dwordx4 v1, s[48:49]
	s_mov_b32 m0, s31
	s_nop 0
	global_load_lds_dwordx4 v1, s[50:51]
	s_mov_b32 m0, s32
	s_nop 0
	global_load_lds_dwordx4 v1, s[52:53]
	s_mov_b32 m0, s33
	s_nop 0
	global_load_lds_dwordx4 v1, s[54:55]
	s_add_u32 s38, s38, 0x80
	s_addc_u32 s39, s39, 0
	s_add_u32 s46, s46, 0x80
	s_addc_u32 s47, s47, 0
	s_add_u32 s48, s48, 0x80
	s_addc_u32 s49, s49, 0
	s_add_u32 s50, s50, 0x80
	s_addc_u32 s51, s51, 0
	s_add_u32 s52, s52, 0x80
	s_addc_u32 s53, s53, 0
	s_add_u32 s54, s54, 0x80
	s_addc_u32 s55, s55, 0
	s_waitcnt lgkmcnt(2)
	v_mfma_f32_16x16x32_f16 v[26:29], v[100:103], v[108:111], v[26:29]
	v_mfma_f32_16x16x32_f16 v[10:13], v[104:107], v[108:111], v[10:13]
	s_waitcnt lgkmcnt(1)
	v_mfma_f32_16x16x32_f16 v[22:25], v[100:103], v[112:115], v[22:25]
	v_mfma_f32_16x16x32_f16 v[6:9], v[104:107], v[112:115], v[6:9]
	s_waitcnt lgkmcnt(0)
	v_mfma_f32_16x16x32_f16 v[30:33], v[100:103], v[116:119], v[30:33]
	v_mfma_f32_16x16x32_f16 v[14:17], v[104:107], v[116:119], v[14:17]
	s_waitcnt vmcnt(0)
	s_barrier
	ds_read_b128 v[100:103], v93 offset:0
	ds_read_b128 v[104:107], v93 offset:2048
	ds_read_b128 v[108:111], v94 offset:16384
	ds_read_b128 v[112:115], v94 offset:18432
	ds_read_b128 v[116:119], v94 offset:20480
	s_waitcnt lgkmcnt(2)
	v_mfma_f32_16x16x32_f16 v[124:127], v[100:103], v[108:111], v[124:127]
	v_mfma_f32_16x16x32_f16 v[62:65], v[104:107], v[108:111], v[62:65]
	ds_read_b128 v[108:111], v94 offset:22528
	s_waitcnt lgkmcnt(2)
	v_mfma_f32_16x16x32_f16 v[86:89], v[100:103], v[112:115], v[86:89]
	v_mfma_f32_16x16x32_f16 v[58:61], v[104:107], v[112:115], v[58:61]
	ds_read_b128 v[112:115], v94 offset:24576
	s_waitcnt lgkmcnt(2)
	v_mfma_f32_16x16x32_f16 v[96:99], v[100:103], v[116:119], v[96:99]
	v_mfma_f32_16x16x32_f16 v[54:57], v[104:107], v[116:119], v[54:57]
	ds_read_b128 v[116:119], v94 offset:26624
	s_waitcnt lgkmcnt(2)
	v_mfma_f32_16x16x32_f16 v[82:85], v[100:103], v[108:111], v[82:85]
	v_mfma_f32_16x16x32_f16 v[50:53], v[104:107], v[108:111], v[50:53]
	ds_read_b128 v[108:111], v94 offset:28672
	s_waitcnt lgkmcnt(2)
	v_mfma_f32_16x16x32_f16 v[78:81], v[100:103], v[112:115], v[78:81]
	v_mfma_f32_16x16x32_f16 v[46:49], v[104:107], v[112:115], v[46:49]
	ds_read_b128 v[112:115], v94 offset:30720
	s_waitcnt lgkmcnt(2)
	v_mfma_f32_16x16x32_f16 v[74:77], v[100:103], v[116:119], v[74:77]
	v_mfma_f32_16x16x32_f16 v[42:45], v[104:107], v[116:119], v[42:45]
	ds_read_b128 v[116:119], v94 offset:32768
	s_waitcnt lgkmcnt(2)
	v_mfma_f32_16x16x32_f16 v[70:73], v[100:103], v[108:111], v[70:73]
	v_mfma_f32_16x16x32_f16 v[38:41], v[104:107], v[108:111], v[38:41]
	ds_read_b128 v[108:111], v94 offset:34816
	s_waitcnt lgkmcnt(2)
	v_mfma_f32_16x16x32_f16 v[66:69], v[100:103], v[112:115], v[66:69]
	v_mfma_f32_16x16x32_f16 v[34:37], v[104:107], v[112:115], v[34:37]
	ds_read_b128 v[112:115], v94 offset:36864
	s_waitcnt lgkmcnt(2)
	v_mfma_f32_16x16x32_f16 v[18:21], v[100:103], v[116:119], v[18:21]
	v_mfma_f32_16x16x32_f16 v[2:5], v[104:107], v[116:119], v[2:5]
	ds_read_b128 v[116:119], v94 offset:38912
	s_waitcnt lgkmcnt(2)
	v_mfma_f32_16x16x32_f16 v[26:29], v[100:103], v[108:111], v[26:29]
	v_mfma_f32_16x16x32_f16 v[10:13], v[104:107], v[108:111], v[10:13]
	v_xor_b32_e32 v94, 64, v94
	ds_read_b128 v[108:111], v94 offset:16384
	s_waitcnt lgkmcnt(2)
	v_mfma_f32_16x16x32_f16 v[22:25], v[100:103], v[112:115], v[22:25]
	v_mfma_f32_16x16x32_f16 v[6:9], v[104:107], v[112:115], v[6:9]
	ds_read_b128 v[112:115], v94 offset:18432
	s_waitcnt lgkmcnt(2)
	v_mfma_f32_16x16x32_f16 v[30:33], v[100:103], v[116:119], v[30:33]
	v_mfma_f32_16x16x32_f16 v[14:17], v[104:107], v[116:119], v[14:17]
	ds_read_b128 v[116:119], v94 offset:20480
	v_xor_b32_e32 v93, 64, v93
	ds_read_b128 v[100:103], v93 offset:0
	ds_read_b128 v[104:107], v93 offset:2048
	v_xor_b32_e32 v93, 64, v93
	s_waitcnt lgkmcnt(0)
	v_mfma_f32_16x16x32_f16 v[124:127], v[100:103], v[108:111], v[124:127]
	v_mfma_f32_16x16x32_f16 v[62:65], v[104:107], v[108:111], v[62:65]
	ds_read_b128 v[108:111], v94 offset:22528
	s_waitcnt lgkmcnt(1)
	v_mfma_f32_16x16x32_f16 v[86:89], v[100:103], v[112:115], v[86:89]
	v_mfma_f32_16x16x32_f16 v[58:61], v[104:107], v[112:115], v[58:61]
	ds_read_b128 v[112:115], v94 offset:24576
	s_waitcnt lgkmcnt(2)
	v_mfma_f32_16x16x32_f16 v[96:99], v[100:103], v[116:119], v[96:99]
	v_mfma_f32_16x16x32_f16 v[54:57], v[104:107], v[116:119], v[54:57]
	ds_read_b128 v[116:119], v94 offset:26624
	s_waitcnt lgkmcnt(2)
	v_mfma_f32_16x16x32_f16 v[82:85], v[100:103], v[108:111], v[82:85]
	v_mfma_f32_16x16x32_f16 v[50:53], v[104:107], v[108:111], v[50:53]
	ds_read_b128 v[108:111], v94 offset:28672
	s_waitcnt lgkmcnt(2)
	v_mfma_f32_16x16x32_f16 v[78:81], v[100:103], v[112:115], v[78:81]
	v_mfma_f32_16x16x32_f16 v[46:49], v[104:107], v[112:115], v[46:49]
	ds_read_b128 v[112:115], v94 offset:30720
	s_waitcnt lgkmcnt(2)
	v_mfma_f32_16x16x32_f16 v[74:77], v[100:103], v[116:119], v[74:77]
	v_mfma_f32_16x16x32_f16 v[42:45], v[104:107], v[116:119], v[42:45]
	ds_read_b128 v[116:119], v94 offset:32768
	s_waitcnt lgkmcnt(2)
	v_mfma_f32_16x16x32_f16 v[70:73], v[100:103], v[108:111], v[70:73]
	v_mfma_f32_16x16x32_f16 v[38:41], v[104:107], v[108:111], v[38:41]
	ds_read_b128 v[108:111], v94 offset:34816
	s_waitcnt lgkmcnt(2)
	v_mfma_f32_16x16x32_f16 v[66:69], v[100:103], v[112:115], v[66:69]
	v_mfma_f32_16x16x32_f16 v[34:37], v[104:107], v[112:115], v[34:37]
	ds_read_b128 v[112:115], v94 offset:36864
	s_waitcnt lgkmcnt(2)
	v_mfma_f32_16x16x32_f16 v[18:21], v[100:103], v[116:119], v[18:21]
	v_mfma_f32_16x16x32_f16 v[2:5], v[104:107], v[116:119], v[2:5]
	ds_read_b128 v[116:119], v94 offset:38912
	v_xor_b32_e32 v94, 64, v94
	s_waitcnt lgkmcnt(0)
	s_barrier
	s_mov_b32 m0, s24
	s_nop 0
	global_load_lds_dwordx4 v120, s[36:37]
	s_mov_b32 m0, s25
	s_nop 0
	global_load_lds_dwordx4 v121, s[36:37]
	s_mov_b32 m0, s26
	s_nop 0
	global_load_lds_dwordx4 v122, s[36:37]
	s_mov_b32 m0, s27
	s_nop 0
	global_load_lds_dwordx4 v123, s[36:37]
	s_add_u32 s36, s36, 0x80
	s_addc_u32 s37, s37, 0
	s_mov_b32 m0, s28
	s_nop 0
	global_load_lds_dwordx4 v1, s[38:39]
	s_mov_b32 m0, s29
	s_nop 0
	global_load_lds_dwordx4 v1, s[46:47]
	s_mov_b32 m0, s30
	s_nop 0
	global_load_lds_dwordx4 v1, s[48:49]
	s_mov_b32 m0, s31
	s_nop 0
	global_load_lds_dwordx4 v1, s[50:51]
	s_mov_b32 m0, s32
	s_nop 0
	global_load_lds_dwordx4 v1, s[52:53]
	s_mov_b32 m0, s33
	s_nop 0
	global_load_lds_dwordx4 v1, s[54:55]
	s_add_u32 s38, s38, 0x80
	s_addc_u32 s39, s39, 0
	s_add_u32 s46, s46, 0x80
	s_addc_u32 s47, s47, 0
	s_add_u32 s48, s48, 0x80
	s_addc_u32 s49, s49, 0
	s_add_u32 s50, s50, 0x80
	s_addc_u32 s51, s51, 0
	s_add_u32 s52, s52, 0x80
	s_addc_u32 s53, s53, 0
	s_add_u32 s54, s54, 0x80
	s_addc_u32 s55, s55, 0
	s_waitcnt lgkmcnt(2)
	v_mfma_f32_16x16x32_f16 v[26:29], v[100:103], v[108:111], v[26:29]
	v_mfma_f32_16x16x32_f16 v[10:13], v[104:107], v[108:111], v[10:13]
	s_waitcnt lgkmcnt(1)
	v_mfma_f32_16x16x32_f16 v[22:25], v[100:103], v[112:115], v[22:25]
	v_mfma_f32_16x16x32_f16 v[6:9], v[104:107], v[112:115], v[6:9]
	s_waitcnt lgkmcnt(0)
	v_mfma_f32_16x16x32_f16 v[30:33], v[100:103], v[116:119], v[30:33]
	v_mfma_f32_16x16x32_f16 v[14:17], v[104:107], v[116:119], v[14:17]
	s_waitcnt vmcnt(0)
	s_barrier
	ds_read_b128 v[100:103], v93 offset:0
	ds_read_b128 v[104:107], v93 offset:2048
	ds_read_b128 v[108:111], v94 offset:16384
	ds_read_b128 v[112:115], v94 offset:18432
	ds_read_b128 v[116:119], v94 offset:20480
	s_waitcnt lgkmcnt(2)
	v_mfma_f32_16x16x32_f16 v[124:127], v[100:103], v[108:111], v[124:127]
	v_mfma_f32_16x16x32_f16 v[62:65], v[104:107], v[108:111], v[62:65]
	ds_read_b128 v[108:111], v94 offset:22528
	s_waitcnt lgkmcnt(2)
	v_mfma_f32_16x16x32_f16 v[86:89], v[100:103], v[112:115], v[86:89]
	v_mfma_f32_16x16x32_f16 v[58:61], v[104:107], v[112:115], v[58:61]
	ds_read_b128 v[112:115], v94 offset:24576
	s_waitcnt lgkmcnt(2)
	v_mfma_f32_16x16x32_f16 v[96:99], v[100:103], v[116:119], v[96:99]
	v_mfma_f32_16x16x32_f16 v[54:57], v[104:107], v[116:119], v[54:57]
	ds_read_b128 v[116:119], v94 offset:26624
	s_waitcnt lgkmcnt(2)
	v_mfma_f32_16x16x32_f16 v[82:85], v[100:103], v[108:111], v[82:85]
	v_mfma_f32_16x16x32_f16 v[50:53], v[104:107], v[108:111], v[50:53]
	ds_read_b128 v[108:111], v94 offset:28672
	s_waitcnt lgkmcnt(2)
	v_mfma_f32_16x16x32_f16 v[78:81], v[100:103], v[112:115], v[78:81]
	v_mfma_f32_16x16x32_f16 v[46:49], v[104:107], v[112:115], v[46:49]
	ds_read_b128 v[112:115], v94 offset:30720
	s_waitcnt lgkmcnt(2)
	v_mfma_f32_16x16x32_f16 v[74:77], v[100:103], v[116:119], v[74:77]
	v_mfma_f32_16x16x32_f16 v[42:45], v[104:107], v[116:119], v[42:45]
	ds_read_b128 v[116:119], v94 offset:32768
	s_waitcnt lgkmcnt(2)
	v_mfma_f32_16x16x32_f16 v[70:73], v[100:103], v[108:111], v[70:73]
	v_mfma_f32_16x16x32_f16 v[38:41], v[104:107], v[108:111], v[38:41]
	ds_read_b128 v[108:111], v94 offset:34816
	s_waitcnt lgkmcnt(2)
	v_mfma_f32_16x16x32_f16 v[66:69], v[100:103], v[112:115], v[66:69]
	v_mfma_f32_16x16x32_f16 v[34:37], v[104:107], v[112:115], v[34:37]
	ds_read_b128 v[112:115], v94 offset:36864
	s_waitcnt lgkmcnt(2)
	v_mfma_f32_16x16x32_f16 v[18:21], v[100:103], v[116:119], v[18:21]
	v_mfma_f32_16x16x32_f16 v[2:5], v[104:107], v[116:119], v[2:5]
	ds_read_b128 v[116:119], v94 offset:38912
	s_waitcnt lgkmcnt(2)
	v_mfma_f32_16x16x32_f16 v[26:29], v[100:103], v[108:111], v[26:29]
	v_mfma_f32_16x16x32_f16 v[10:13], v[104:107], v[108:111], v[10:13]
	v_xor_b32_e32 v94, 64, v94
	ds_read_b128 v[108:111], v94 offset:16384
	s_waitcnt lgkmcnt(2)
	v_mfma_f32_16x16x32_f16 v[22:25], v[100:103], v[112:115], v[22:25]
	v_mfma_f32_16x16x32_f16 v[6:9], v[104:107], v[112:115], v[6:9]
	ds_read_b128 v[112:115], v94 offset:18432
	s_waitcnt lgkmcnt(2)
	v_mfma_f32_16x16x32_f16 v[30:33], v[100:103], v[116:119], v[30:33]
	v_mfma_f32_16x16x32_f16 v[14:17], v[104:107], v[116:119], v[14:17]
	ds_read_b128 v[116:119], v94 offset:20480
	v_xor_b32_e32 v93, 64, v93
	ds_read_b128 v[100:103], v93 offset:0
	ds_read_b128 v[104:107], v93 offset:2048
	v_xor_b32_e32 v93, 64, v93
	s_waitcnt lgkmcnt(0)
	v_mfma_f32_16x16x32_f16 v[124:127], v[100:103], v[108:111], v[124:127]
	v_mfma_f32_16x16x32_f16 v[62:65], v[104:107], v[108:111], v[62:65]
	ds_read_b128 v[108:111], v94 offset:22528
	s_waitcnt lgkmcnt(1)
	v_mfma_f32_16x16x32_f16 v[86:89], v[100:103], v[112:115], v[86:89]
	v_mfma_f32_16x16x32_f16 v[58:61], v[104:107], v[112:115], v[58:61]
	ds_read_b128 v[112:115], v94 offset:24576
	s_waitcnt lgkmcnt(2)
	v_mfma_f32_16x16x32_f16 v[96:99], v[100:103], v[116:119], v[96:99]
	v_mfma_f32_16x16x32_f16 v[54:57], v[104:107], v[116:119], v[54:57]
	ds_read_b128 v[116:119], v94 offset:26624
	s_waitcnt lgkmcnt(2)
	v_mfma_f32_16x16x32_f16 v[82:85], v[100:103], v[108:111], v[82:85]
	v_mfma_f32_16x16x32_f16 v[50:53], v[104:107], v[108:111], v[50:53]
	ds_read_b128 v[108:111], v94 offset:28672
	s_waitcnt lgkmcnt(2)
	v_mfma_f32_16x16x32_f16 v[78:81], v[100:103], v[112:115], v[78:81]
	v_mfma_f32_16x16x32_f16 v[46:49], v[104:107], v[112:115], v[46:49]
	ds_read_b128 v[112:115], v94 offset:30720
	s_waitcnt lgkmcnt(2)
	v_mfma_f32_16x16x32_f16 v[74:77], v[100:103], v[116:119], v[74:77]
	v_mfma_f32_16x16x32_f16 v[42:45], v[104:107], v[116:119], v[42:45]
	ds_read_b128 v[116:119], v94 offset:32768
	s_waitcnt lgkmcnt(2)
	v_mfma_f32_16x16x32_f16 v[70:73], v[100:103], v[108:111], v[70:73]
	v_mfma_f32_16x16x32_f16 v[38:41], v[104:107], v[108:111], v[38:41]
	ds_read_b128 v[108:111], v94 offset:34816
	s_waitcnt lgkmcnt(2)
	v_mfma_f32_16x16x32_f16 v[66:69], v[100:103], v[112:115], v[66:69]
	v_mfma_f32_16x16x32_f16 v[34:37], v[104:107], v[112:115], v[34:37]
	ds_read_b128 v[112:115], v94 offset:36864
	s_waitcnt lgkmcnt(2)
	v_mfma_f32_16x16x32_f16 v[18:21], v[100:103], v[116:119], v[18:21]
	v_mfma_f32_16x16x32_f16 v[2:5], v[104:107], v[116:119], v[2:5]
	ds_read_b128 v[116:119], v94 offset:38912
	v_xor_b32_e32 v94, 64, v94
	s_waitcnt lgkmcnt(0)
	s_barrier
	s_mov_b32 m0, s24
	s_nop 0
	global_load_lds_dwordx4 v120, s[36:37]
	s_mov_b32 m0, s25
	s_nop 0
	global_load_lds_dwordx4 v121, s[36:37]
	s_mov_b32 m0, s26
	s_nop 0
	global_load_lds_dwordx4 v122, s[36:37]
	s_mov_b32 m0, s27
	s_nop 0
	global_load_lds_dwordx4 v123, s[36:37]
	s_add_u32 s36, s36, 0x80
	s_addc_u32 s37, s37, 0
	s_mov_b32 m0, s28
	s_nop 0
	global_load_lds_dwordx4 v1, s[38:39]
	s_mov_b32 m0, s29
	s_nop 0
	global_load_lds_dwordx4 v1, s[46:47]
	s_mov_b32 m0, s30
	s_nop 0
	global_load_lds_dwordx4 v1, s[48:49]
	s_mov_b32 m0, s31
	s_nop 0
	global_load_lds_dwordx4 v1, s[50:51]
	s_mov_b32 m0, s32
	s_nop 0
	global_load_lds_dwordx4 v1, s[52:53]
	s_mov_b32 m0, s33
	s_nop 0
	global_load_lds_dwordx4 v1, s[54:55]
	s_add_u32 s38, s38, 0x80
	s_addc_u32 s39, s39, 0
	s_add_u32 s46, s46, 0x80
	s_addc_u32 s47, s47, 0
	s_add_u32 s48, s48, 0x80
	s_addc_u32 s49, s49, 0
	s_add_u32 s50, s50, 0x80
	s_addc_u32 s51, s51, 0
	s_add_u32 s52, s52, 0x80
	s_addc_u32 s53, s53, 0
	s_add_u32 s54, s54, 0x80
	s_addc_u32 s55, s55, 0
	s_waitcnt lgkmcnt(2)
	v_mfma_f32_16x16x32_f16 v[26:29], v[100:103], v[108:111], v[26:29]
	v_mfma_f32_16x16x32_f16 v[10:13], v[104:107], v[108:111], v[10:13]
	s_waitcnt lgkmcnt(1)
	v_mfma_f32_16x16x32_f16 v[22:25], v[100:103], v[112:115], v[22:25]
	v_mfma_f32_16x16x32_f16 v[6:9], v[104:107], v[112:115], v[6:9]
	s_waitcnt lgkmcnt(0)
	v_mfma_f32_16x16x32_f16 v[30:33], v[100:103], v[116:119], v[30:33]
	v_mfma_f32_16x16x32_f16 v[14:17], v[104:107], v[116:119], v[14:17]
	s_waitcnt vmcnt(0)
	s_barrier
	ds_read_b128 v[100:103], v93 offset:0
	ds_read_b128 v[104:107], v93 offset:2048
	ds_read_b128 v[108:111], v94 offset:16384
	ds_read_b128 v[112:115], v94 offset:18432
	ds_read_b128 v[116:119], v94 offset:20480
	s_waitcnt lgkmcnt(2)
	v_mfma_f32_16x16x32_f16 v[124:127], v[100:103], v[108:111], v[124:127]
	v_mfma_f32_16x16x32_f16 v[62:65], v[104:107], v[108:111], v[62:65]
	ds_read_b128 v[108:111], v94 offset:22528
	s_waitcnt lgkmcnt(2)
	v_mfma_f32_16x16x32_f16 v[86:89], v[100:103], v[112:115], v[86:89]
	v_mfma_f32_16x16x32_f16 v[58:61], v[104:107], v[112:115], v[58:61]
	ds_read_b128 v[112:115], v94 offset:24576
	s_waitcnt lgkmcnt(2)
	v_mfma_f32_16x16x32_f16 v[96:99], v[100:103], v[116:119], v[96:99]
	v_mfma_f32_16x16x32_f16 v[54:57], v[104:107], v[116:119], v[54:57]
	ds_read_b128 v[116:119], v94 offset:26624
	s_waitcnt lgkmcnt(2)
	v_mfma_f32_16x16x32_f16 v[82:85], v[100:103], v[108:111], v[82:85]
	v_mfma_f32_16x16x32_f16 v[50:53], v[104:107], v[108:111], v[50:53]
	ds_read_b128 v[108:111], v94 offset:28672
	s_waitcnt lgkmcnt(2)
	v_mfma_f32_16x16x32_f16 v[78:81], v[100:103], v[112:115], v[78:81]
	v_mfma_f32_16x16x32_f16 v[46:49], v[104:107], v[112:115], v[46:49]
	ds_read_b128 v[112:115], v94 offset:30720
	s_waitcnt lgkmcnt(2)
	v_mfma_f32_16x16x32_f16 v[74:77], v[100:103], v[116:119], v[74:77]
	v_mfma_f32_16x16x32_f16 v[42:45], v[104:107], v[116:119], v[42:45]
	ds_read_b128 v[116:119], v94 offset:32768
	s_waitcnt lgkmcnt(2)
	v_mfma_f32_16x16x32_f16 v[70:73], v[100:103], v[108:111], v[70:73]
	v_mfma_f32_16x16x32_f16 v[38:41], v[104:107], v[108:111], v[38:41]
	ds_read_b128 v[108:111], v94 offset:34816
	s_waitcnt lgkmcnt(2)
	v_mfma_f32_16x16x32_f16 v[66:69], v[100:103], v[112:115], v[66:69]
	v_mfma_f32_16x16x32_f16 v[34:37], v[104:107], v[112:115], v[34:37]
	ds_read_b128 v[112:115], v94 offset:36864
	s_waitcnt lgkmcnt(2)
	v_mfma_f32_16x16x32_f16 v[18:21], v[100:103], v[116:119], v[18:21]
	v_mfma_f32_16x16x32_f16 v[2:5], v[104:107], v[116:119], v[2:5]
	ds_read_b128 v[116:119], v94 offset:38912
	s_waitcnt lgkmcnt(2)
	v_mfma_f32_16x16x32_f16 v[26:29], v[100:103], v[108:111], v[26:29]
	v_mfma_f32_16x16x32_f16 v[10:13], v[104:107], v[108:111], v[10:13]
	v_xor_b32_e32 v94, 64, v94
	ds_read_b128 v[108:111], v94 offset:16384
	s_waitcnt lgkmcnt(2)
	v_mfma_f32_16x16x32_f16 v[22:25], v[100:103], v[112:115], v[22:25]
	v_mfma_f32_16x16x32_f16 v[6:9], v[104:107], v[112:115], v[6:9]
	ds_read_b128 v[112:115], v94 offset:18432
	s_waitcnt lgkmcnt(2)
	v_mfma_f32_16x16x32_f16 v[30:33], v[100:103], v[116:119], v[30:33]
	v_mfma_f32_16x16x32_f16 v[14:17], v[104:107], v[116:119], v[14:17]
	ds_read_b128 v[116:119], v94 offset:20480
	v_xor_b32_e32 v93, 64, v93
	ds_read_b128 v[100:103], v93 offset:0
	ds_read_b128 v[104:107], v93 offset:2048
	v_xor_b32_e32 v93, 64, v93
	s_waitcnt lgkmcnt(0)
	v_mfma_f32_16x16x32_f16 v[124:127], v[100:103], v[108:111], v[124:127]
	v_mfma_f32_16x16x32_f16 v[62:65], v[104:107], v[108:111], v[62:65]
	ds_read_b128 v[108:111], v94 offset:22528
	s_waitcnt lgkmcnt(1)
	v_mfma_f32_16x16x32_f16 v[86:89], v[100:103], v[112:115], v[86:89]
	v_mfma_f32_16x16x32_f16 v[58:61], v[104:107], v[112:115], v[58:61]
	ds_read_b128 v[112:115], v94 offset:24576
	s_waitcnt lgkmcnt(2)
	v_mfma_f32_16x16x32_f16 v[96:99], v[100:103], v[116:119], v[96:99]
	v_mfma_f32_16x16x32_f16 v[54:57], v[104:107], v[116:119], v[54:57]
	ds_read_b128 v[116:119], v94 offset:26624
	s_waitcnt lgkmcnt(2)
	v_mfma_f32_16x16x32_f16 v[82:85], v[100:103], v[108:111], v[82:85]
	v_mfma_f32_16x16x32_f16 v[50:53], v[104:107], v[108:111], v[50:53]
	ds_read_b128 v[108:111], v94 offset:28672
	s_waitcnt lgkmcnt(2)
	v_mfma_f32_16x16x32_f16 v[78:81], v[100:103], v[112:115], v[78:81]
	v_mfma_f32_16x16x32_f16 v[46:49], v[104:107], v[112:115], v[46:49]
	ds_read_b128 v[112:115], v94 offset:30720
	s_waitcnt lgkmcnt(2)
	v_mfma_f32_16x16x32_f16 v[74:77], v[100:103], v[116:119], v[74:77]
	v_mfma_f32_16x16x32_f16 v[42:45], v[104:107], v[116:119], v[42:45]
	ds_read_b128 v[116:119], v94 offset:32768
	s_waitcnt lgkmcnt(2)
	v_mfma_f32_16x16x32_f16 v[70:73], v[100:103], v[108:111], v[70:73]
	v_mfma_f32_16x16x32_f16 v[38:41], v[104:107], v[108:111], v[38:41]
	ds_read_b128 v[108:111], v94 offset:34816
	s_waitcnt lgkmcnt(2)
	v_mfma_f32_16x16x32_f16 v[66:69], v[100:103], v[112:115], v[66:69]
	v_mfma_f32_16x16x32_f16 v[34:37], v[104:107], v[112:115], v[34:37]
	ds_read_b128 v[112:115], v94 offset:36864
	s_waitcnt lgkmcnt(2)
	v_mfma_f32_16x16x32_f16 v[18:21], v[100:103], v[116:119], v[18:21]
	v_mfma_f32_16x16x32_f16 v[2:5], v[104:107], v[116:119], v[2:5]
	ds_read_b128 v[116:119], v94 offset:38912
	v_xor_b32_e32 v94, 64, v94
	s_waitcnt lgkmcnt(0)
	s_barrier
	s_mov_b32 m0, s24
	s_nop 0
	global_load_lds_dwordx4 v120, s[36:37]
	s_mov_b32 m0, s25
	s_nop 0
	global_load_lds_dwordx4 v121, s[36:37]
	s_mov_b32 m0, s26
	s_nop 0
	global_load_lds_dwordx4 v122, s[36:37]
	s_mov_b32 m0, s27
	s_nop 0
	global_load_lds_dwordx4 v123, s[36:37]
	s_add_u32 s36, s36, 0x80
	s_addc_u32 s37, s37, 0
	s_mov_b32 m0, s28
	s_nop 0
	global_load_lds_dwordx4 v1, s[38:39]
	s_mov_b32 m0, s29
	s_nop 0
	global_load_lds_dwordx4 v1, s[46:47]
	s_mov_b32 m0, s30
	s_nop 0
	global_load_lds_dwordx4 v1, s[48:49]
	s_mov_b32 m0, s31
	s_nop 0
	global_load_lds_dwordx4 v1, s[50:51]
	s_mov_b32 m0, s32
	s_nop 0
	global_load_lds_dwordx4 v1, s[52:53]
	s_mov_b32 m0, s33
	s_nop 0
	global_load_lds_dwordx4 v1, s[54:55]
	s_add_u32 s38, s38, 0x80
	s_addc_u32 s39, s39, 0
	s_add_u32 s46, s46, 0x80
	s_addc_u32 s47, s47, 0
	s_add_u32 s48, s48, 0x80
	s_addc_u32 s49, s49, 0
	s_add_u32 s50, s50, 0x80
	s_addc_u32 s51, s51, 0
	s_add_u32 s52, s52, 0x80
	s_addc_u32 s53, s53, 0
	s_add_u32 s54, s54, 0x80
	s_addc_u32 s55, s55, 0
	s_waitcnt lgkmcnt(2)
	v_mfma_f32_16x16x32_f16 v[26:29], v[100:103], v[108:111], v[26:29]
	v_mfma_f32_16x16x32_f16 v[10:13], v[104:107], v[108:111], v[10:13]
	s_waitcnt lgkmcnt(1)
	v_mfma_f32_16x16x32_f16 v[22:25], v[100:103], v[112:115], v[22:25]
	v_mfma_f32_16x16x32_f16 v[6:9], v[104:107], v[112:115], v[6:9]
	s_waitcnt lgkmcnt(0)
	v_mfma_f32_16x16x32_f16 v[30:33], v[100:103], v[116:119], v[30:33]
	v_mfma_f32_16x16x32_f16 v[14:17], v[104:107], v[116:119], v[14:17]
	s_waitcnt vmcnt(0)
	s_barrier
	ds_read_b128 v[100:103], v93 offset:0
	ds_read_b128 v[104:107], v93 offset:2048
	ds_read_b128 v[108:111], v94 offset:16384
	ds_read_b128 v[112:115], v94 offset:18432
	ds_read_b128 v[116:119], v94 offset:20480
	s_waitcnt lgkmcnt(2)
	v_mfma_f32_16x16x32_f16 v[124:127], v[100:103], v[108:111], v[124:127]
	v_mfma_f32_16x16x32_f16 v[62:65], v[104:107], v[108:111], v[62:65]
	ds_read_b128 v[108:111], v94 offset:22528
	s_waitcnt lgkmcnt(2)
	v_mfma_f32_16x16x32_f16 v[86:89], v[100:103], v[112:115], v[86:89]
	v_mfma_f32_16x16x32_f16 v[58:61], v[104:107], v[112:115], v[58:61]
	ds_read_b128 v[112:115], v94 offset:24576
	s_waitcnt lgkmcnt(2)
	v_mfma_f32_16x16x32_f16 v[96:99], v[100:103], v[116:119], v[96:99]
	v_mfma_f32_16x16x32_f16 v[54:57], v[104:107], v[116:119], v[54:57]
	ds_read_b128 v[116:119], v94 offset:26624
	s_waitcnt lgkmcnt(2)
	v_mfma_f32_16x16x32_f16 v[82:85], v[100:103], v[108:111], v[82:85]
	v_mfma_f32_16x16x32_f16 v[50:53], v[104:107], v[108:111], v[50:53]
	ds_read_b128 v[108:111], v94 offset:28672
	s_waitcnt lgkmcnt(2)
	v_mfma_f32_16x16x32_f16 v[78:81], v[100:103], v[112:115], v[78:81]
	v_mfma_f32_16x16x32_f16 v[46:49], v[104:107], v[112:115], v[46:49]
	ds_read_b128 v[112:115], v94 offset:30720
	s_waitcnt lgkmcnt(2)
	v_mfma_f32_16x16x32_f16 v[74:77], v[100:103], v[116:119], v[74:77]
	v_mfma_f32_16x16x32_f16 v[42:45], v[104:107], v[116:119], v[42:45]
	ds_read_b128 v[116:119], v94 offset:32768
	s_waitcnt lgkmcnt(2)
	v_mfma_f32_16x16x32_f16 v[70:73], v[100:103], v[108:111], v[70:73]
	v_mfma_f32_16x16x32_f16 v[38:41], v[104:107], v[108:111], v[38:41]
	ds_read_b128 v[108:111], v94 offset:34816
	s_waitcnt lgkmcnt(2)
	v_mfma_f32_16x16x32_f16 v[66:69], v[100:103], v[112:115], v[66:69]
	v_mfma_f32_16x16x32_f16 v[34:37], v[104:107], v[112:115], v[34:37]
	ds_read_b128 v[112:115], v94 offset:36864
	s_waitcnt lgkmcnt(2)
	v_mfma_f32_16x16x32_f16 v[18:21], v[100:103], v[116:119], v[18:21]
	v_mfma_f32_16x16x32_f16 v[2:5], v[104:107], v[116:119], v[2:5]
	ds_read_b128 v[116:119], v94 offset:38912
	s_waitcnt lgkmcnt(2)
	v_mfma_f32_16x16x32_f16 v[26:29], v[100:103], v[108:111], v[26:29]
	v_mfma_f32_16x16x32_f16 v[10:13], v[104:107], v[108:111], v[10:13]
	v_xor_b32_e32 v94, 64, v94
	ds_read_b128 v[108:111], v94 offset:16384
	s_waitcnt lgkmcnt(2)
	v_mfma_f32_16x16x32_f16 v[22:25], v[100:103], v[112:115], v[22:25]
	v_mfma_f32_16x16x32_f16 v[6:9], v[104:107], v[112:115], v[6:9]
	ds_read_b128 v[112:115], v94 offset:18432
	s_waitcnt lgkmcnt(2)
	v_mfma_f32_16x16x32_f16 v[30:33], v[100:103], v[116:119], v[30:33]
	v_mfma_f32_16x16x32_f16 v[14:17], v[104:107], v[116:119], v[14:17]
	ds_read_b128 v[116:119], v94 offset:20480
	v_xor_b32_e32 v93, 64, v93
	ds_read_b128 v[100:103], v93 offset:0
	ds_read_b128 v[104:107], v93 offset:2048
	v_xor_b32_e32 v93, 64, v93
	s_waitcnt lgkmcnt(0)
	v_mfma_f32_16x16x32_f16 v[124:127], v[100:103], v[108:111], v[124:127]
	v_mfma_f32_16x16x32_f16 v[62:65], v[104:107], v[108:111], v[62:65]
	ds_read_b128 v[108:111], v94 offset:22528
	s_waitcnt lgkmcnt(1)
	v_mfma_f32_16x16x32_f16 v[86:89], v[100:103], v[112:115], v[86:89]
	v_mfma_f32_16x16x32_f16 v[58:61], v[104:107], v[112:115], v[58:61]
	ds_read_b128 v[112:115], v94 offset:24576
	s_waitcnt lgkmcnt(2)
	v_mfma_f32_16x16x32_f16 v[96:99], v[100:103], v[116:119], v[96:99]
	v_mfma_f32_16x16x32_f16 v[54:57], v[104:107], v[116:119], v[54:57]
	ds_read_b128 v[116:119], v94 offset:26624
	s_waitcnt lgkmcnt(2)
	v_mfma_f32_16x16x32_f16 v[82:85], v[100:103], v[108:111], v[82:85]
	v_mfma_f32_16x16x32_f16 v[50:53], v[104:107], v[108:111], v[50:53]
	ds_read_b128 v[108:111], v94 offset:28672
	s_waitcnt lgkmcnt(2)
	v_mfma_f32_16x16x32_f16 v[78:81], v[100:103], v[112:115], v[78:81]
	v_mfma_f32_16x16x32_f16 v[46:49], v[104:107], v[112:115], v[46:49]
	ds_read_b128 v[112:115], v94 offset:30720
	s_waitcnt lgkmcnt(2)
	v_mfma_f32_16x16x32_f16 v[74:77], v[100:103], v[116:119], v[74:77]
	v_mfma_f32_16x16x32_f16 v[42:45], v[104:107], v[116:119], v[42:45]
	ds_read_b128 v[116:119], v94 offset:32768
	s_waitcnt lgkmcnt(2)
	v_mfma_f32_16x16x32_f16 v[70:73], v[100:103], v[108:111], v[70:73]
	v_mfma_f32_16x16x32_f16 v[38:41], v[104:107], v[108:111], v[38:41]
	ds_read_b128 v[108:111], v94 offset:34816
	s_waitcnt lgkmcnt(2)
	v_mfma_f32_16x16x32_f16 v[66:69], v[100:103], v[112:115], v[66:69]
	v_mfma_f32_16x16x32_f16 v[34:37], v[104:107], v[112:115], v[34:37]
	ds_read_b128 v[112:115], v94 offset:36864
	s_waitcnt lgkmcnt(2)
	v_mfma_f32_16x16x32_f16 v[18:21], v[100:103], v[116:119], v[18:21]
	v_mfma_f32_16x16x32_f16 v[2:5], v[104:107], v[116:119], v[2:5]
	ds_read_b128 v[116:119], v94 offset:38912
	v_xor_b32_e32 v94, 64, v94
	s_waitcnt lgkmcnt(0)
	s_barrier
	s_waitcnt lgkmcnt(2)
	v_mfma_f32_16x16x32_f16 v[26:29], v[100:103], v[108:111], v[26:29]
	v_mfma_f32_16x16x32_f16 v[10:13], v[104:107], v[108:111], v[10:13]
	s_waitcnt lgkmcnt(1)
	v_mfma_f32_16x16x32_f16 v[22:25], v[100:103], v[112:115], v[22:25]
	v_mfma_f32_16x16x32_f16 v[6:9], v[104:107], v[112:115], v[6:9]
	s_waitcnt lgkmcnt(0)
	v_mfma_f32_16x16x32_f16 v[30:33], v[100:103], v[116:119], v[30:33]
	v_mfma_f32_16x16x32_f16 v[14:17], v[104:107], v[116:119], v[14:17]
	s_nop 15
	s_nop 15
	v_lshrrev_b32_e32 v1, 6, v0
	s_movk_i32 s2, 0xfc
	v_cmp_gt_u32_e32 vcc, s2, v0
	s_mov_b32 s2, 0x12492493
	s_movk_i32 s4, 0x380
	s_movk_i32 s12, 0x110
	v_cmp_gt_u32_e64 s[4:5], s4, v0
	v_lshrrev_b32_e32 v93, 1, v0
	v_cndmask_b32_e32 v94, 0, v93, vcc
	s_nop 5
	v_cvt_f16_f32_e32 v86, v86
	s_nop 5
	v_cvt_f16_f32_e32 v54, v54
	v_cvt_f16_f32_e32 v82, v82
	v_cvt_f16_f32_e32 v50, v50
	s_nop 5
	v_cvt_f16_f32_e32 v78, v78
	v_mul_i32_i24_e32 v102, 0xffffffc2, v92
	v_mul_u32_u24_e32 v101, 0x110, v91
	v_lshlrev_b32_e32 v91, 6, v92
	v_add3_u32 v91, v91, v102, v101
	ds_write_b16 v91, v86 offset:32
	v_cvt_f16_f32_e32 v86, v87
	v_cvt_f16_f32_e32 v74, v74
	v_cvt_f16_f32_e32 v102, v125
	ds_write_b16 v91, v86 offset:304
	v_cvt_f16_f32_e32 v86, v88
	s_nop 2
	v_cvt_f16_f32_e32 v34, v34
	ds_write_b16 v91, v82 offset:96
	ds_write_b16 v91, v86 offset:576
	v_cvt_f16_f32_e32 v86, v89
	v_cvt_f16_f32_e32 v38, v38
	ds_write_b16 v91, v34 offset:4576
	ds_write_b16 v91, v86 offset:848
	v_cvt_f16_f32_e32 v86, v96
	s_nop 1
	v_cvt_f16_f32_e32 v62, v62
	v_cvt_f16_f32_e32 v34, v35
	s_nop 0
	v_cvt_f16_f32_e32 v58, v58
	ds_write_b16 v91, v38 offset:4544
	v_cvt_f16_f32_e32 v38, v39
	s_nop 1
	v_cvt_f16_f32_e32 v46, v46
	ds_write_b16 v91, v86 offset:64
	v_cvt_f16_f32_e32 v86, v97
	s_nop 0
	v_cvt_f16_f32_e32 v42, v42
	v_cvt_f16_f32_e32 v82, v83
	ds_write_b16 v91, v78 offset:128
	s_nop 1
	v_cvt_f16_f32_e32 v70, v70
	v_cvt_f16_f32_e32 v78, v79
	ds_write_b16 v91, v74 offset:160
	v_cvt_f16_f32_e32 v74, v75
	s_nop 0
	v_cvt_f16_f32_e32 v66, v66
	ds_write_b16 v91, v70 offset:192
	v_cvt_f16_f32_e32 v70, v71
	ds_write_b16 v91, v62 offset:4352
	ds_write_b16 v91, v66 offset:224
	v_cvt_f16_f32_e32 v66, v67
	v_cvt_f16_f32_e32 v62, v63
	ds_write_b16 v91, v58 offset:4384
	v_cvt_f16_f32_e32 v58, v59
	ds_write_b16 v91, v54 offset:4416
	v_cvt_f16_f32_e32 v54, v55
	ds_write_b16 v91, v50 offset:4448
	v_cvt_f16_f32_e32 v50, v51
	ds_write_b16 v91, v46 offset:4480
	v_cvt_f16_f32_e32 v46, v47
	ds_write_b16 v91, v42 offset:4512
	v_cvt_f16_f32_e32 v42, v43
	ds_write_b16 v91, v34 offset:4848
	v_cvt_f16_f32_e32 v34, v36
	ds_write_b16 v91, v38 offset:4816
	v_cvt_f16_f32_e32 v38, v40
	ds_write_b16 v91, v102 offset:272
	v_cvt_f16_f32_e32 v102, v126
	ds_write_b16 v91, v86 offset:336
	v_cvt_f16_f32_e32 v86, v98
	ds_write_b16 v91, v82 offset:368
	v_cvt_f16_f32_e32 v82, v84
	ds_write_b16 v91, v78 offset:400
	v_cvt_f16_f32_e32 v78, v80
	ds_write_b16 v91, v74 offset:432
	v_cvt_f16_f32_e32 v74, v76
	ds_write_b16 v91, v70 offset:464
	v_cvt_f16_f32_e32 v70, v72
	ds_write_b16 v91, v66 offset:496
	v_cvt_f16_f32_e32 v66, v68
	ds_write_b16 v91, v62 offset:4624
	v_cvt_f16_f32_e32 v62, v64
	ds_write_b16 v91, v58 offset:4656
	v_cvt_f16_f32_e32 v58, v60
	ds_write_b16 v91, v54 offset:4688
	v_cvt_f16_f32_e32 v54, v56
	ds_write_b16 v91, v50 offset:4720
	v_cvt_f16_f32_e32 v50, v52
	ds_write_b16 v91, v46 offset:4752
	v_cvt_f16_f32_e32 v46, v48
	ds_write_b16 v91, v42 offset:4784
	v_cvt_f16_f32_e32 v42, v44
	ds_write_b16 v91, v34 offset:5120
	v_cvt_f16_f32_e32 v34, v37
	ds_write_b16 v91, v38 offset:5088
	v_cvt_f16_f32_e32 v38, v41
	v_cvt_f16_f32_e32 v103, v124
	ds_write_b16 v91, v102 offset:544
	v_cvt_f16_f32_e32 v102, v127
	ds_write_b16 v91, v86 offset:608
	v_cvt_f16_f32_e32 v86, v99
	ds_write_b16 v91, v82 offset:640
	v_cvt_f16_f32_e32 v82, v85
	ds_write_b16 v91, v78 offset:672
	v_cvt_f16_f32_e32 v78, v81
	ds_write_b16 v91, v74 offset:704
	v_cvt_f16_f32_e32 v74, v77
	ds_write_b16 v91, v70 offset:736
	v_cvt_f16_f32_e32 v70, v73
	ds_write_b16 v91, v66 offset:768
	v_cvt_f16_f32_e32 v66, v69
	ds_write_b16 v91, v62 offset:4896
	v_cvt_f16_f32_e32 v62, v65
	ds_write_b16 v91, v58 offset:4928
	v_cvt_f16_f32_e32 v58, v61
	ds_write_b16 v91, v54 offset:4960
	v_cvt_f16_f32_e32 v54, v57
	ds_write_b16 v91, v50 offset:4992
	v_cvt_f16_f32_e32 v50, v53
	ds_write_b16 v91, v46 offset:5024
	v_cvt_f16_f32_e32 v46, v49
	ds_write_b16 v91, v42 offset:5056
	v_cvt_f16_f32_e32 v42, v45
	ds_write_b16 v91, v34 offset:5392
	v_min_u32_e32 v34, 8, v92
	v_mul_hi_u32 v100, v94, s2
	ds_write_b16 v91, v38 offset:5360
	v_cmp_gt_u32_e64 s[2:3], 9, v92
	v_mul_u32_u24_e32 v39, 14, v34
	v_and_b32_e32 v40, 48, v0
	v_lshlrev_b32_e32 v38, 2, v92
	ds_write_b16 v91, v103
	ds_write_b16 v91, v102 offset:816
	ds_write_b16 v91, v86 offset:880
	ds_write_b16 v91, v82 offset:912
	ds_write_b16 v91, v78 offset:944
	ds_write_b16 v91, v74 offset:976
	ds_write_b16 v91, v70 offset:1008
	ds_write_b16 v91, v66 offset:1040
	ds_write_b16 v91, v62 offset:5168
	ds_write_b16 v91, v58 offset:5200
	ds_write_b16 v91, v54 offset:5232
	ds_write_b16 v91, v50 offset:5264
	ds_write_b16 v91, v46 offset:5296
	ds_write_b16 v91, v42 offset:5328
	s_waitcnt lgkmcnt(0)
	s_barrier
	s_and_saveexec_b64 s[6:7], s[4:5]
	s_cbranch_execz .LBB1_9
	v_add_u32_e32 v34, v1, v39
	v_mad_u32_u24 v41, v34, s12, v40
	ds_read_b128 v[34:37], v41
	ds_read_b128 v[42:45], v41 offset:64
	ds_read_b128 v[46:49], v41 offset:128
	ds_read_b128 v[50:53], v41 offset:192
	v_cmp_ne_u32_e64 s[4:5], 3, v90
	v_mul_u32_u24_e32 v41, 9, v1
	s_and_b64 s[12:13], s[4:5], s[2:3]
	s_waitcnt lgkmcnt(1)
	v_mfma_f32_16x16x32_f16 v[34:37], v[34:37], v[46:49], 0
	s_waitcnt lgkmcnt(0)
	v_mfma_f32_16x16x32_f16 v[34:37], v[42:45], v[50:53], v[34:37]
	s_and_saveexec_b64 s[4:5], s[12:13]
	v_add_u32_e32 v42, v95, v41
	s_nop 5
	v_mul_f32_e32 v34, 0x3e000000, v34
	v_mad_u32_u24 v42, v42, 48, v38
	ds_write_b32 v42, v34 offset:34816
	s_or_b64 exec, exec, s[4:5]
	v_or_b32_e32 v34, 1, v95
	v_cmp_gt_u32_e64 s[4:5], 9, v34
	s_and_b64 s[12:13], s[4:5], s[2:3]
	s_and_saveexec_b64 s[4:5], s[12:13]
	v_add_u32_e32 v34, v34, v41
	v_mul_f32_e32 v35, 0x3e000000, v35
	v_mad_u32_u24 v34, v34, 48, v38
	ds_write_b32 v34, v35 offset:34816
	s_or_b64 exec, exec, s[4:5]
	v_or_b32_e32 v34, 2, v95
	v_cmp_gt_u32_e64 s[4:5], 9, v34
	s_and_b64 s[12:13], s[4:5], s[2:3]
	s_and_saveexec_b64 s[4:5], s[12:13]
	v_add_u32_e32 v34, v34, v41
	v_mul_f32_e32 v35, 0x3e000000, v36
	v_mad_u32_u24 v34, v34, 48, v38
	ds_write_b32 v34, v35 offset:34816
	s_or_b64 exec, exec, s[4:5]
	v_or_b32_e32 v34, 3, v95
	v_cmp_gt_u32_e64 s[4:5], 9, v34
	s_and_b64 s[4:5], s[4:5], s[2:3]
	s_and_b64 exec, exec, s[4:5]
	v_add_u32_e32 v34, v34, v41
	v_mul_f32_e32 v35, 0x3e000000, v37
	v_mad_u32_u24 v34, v34, 48, v38
	ds_write_b32 v34, v35 offset:34816
